# rwkv_pre S4 rewritten: wave-uniform types, LDS reads software-pipelined; prefetch-load wait moved before S4 stores
# speedup vs baseline: 1.0043x; 1.0043x over previous
.LBB0_600:
	v_mov_b64_e32 v[22:23], v[38:39]
	v_mov_b64_e32 v[18:19], v[42:43]
	v_mov_b64_e32 v[30:31], v[46:47]
	v_mov_b64_e32 v[26:27], v[50:51]
	v_mov_b64_e32 v[176:177], v[56:57]
	v_mov_b64_e32 v[168:169], v[60:61]
	v_mov_b64_e32 v[180:181], v[64:65]
	v_mov_b64_e32 v[172:173], v[68:69]
	s_and_b64 vcc, exec, s[8:9]
	v_mov_b64_e32 v[24:25], v[40:41]
	v_mov_b64_e32 v[20:21], v[44:45]
	v_mov_b64_e32 v[32:33], v[48:49]
	v_mov_b64_e32 v[28:29], v[52:53]
	v_mov_b64_e32 v[174:175], v[54:55]
	v_mov_b64_e32 v[166:167], v[58:59]
	v_mov_b64_e32 v[178:179], v[62:63]
	v_mov_b64_e32 v[170:171], v[66:67]
	v_mov_b32_e32 v240, v224
	v_mov_b32_e32 v241, v225
	v_mov_b32_e32 v242, v226
	v_mov_b32_e32 v243, v227
	v_mov_b32_e32 v244, v229
	v_mov_b32_e32 v245, v231
	v_mov_b32_e32 v246, v232
	v_mov_b32_e32 v247, v234
	s_mov_b32 s10, s38
	s_cbranch_vccnz .LBB0_654

.LBB0_638:
	v_mov_b32_e32 v0, v187
	s_ashr_i32 s11, s10, 31
	s_barrier
	s_waitcnt vmcnt(0)
	s_lshl_b64 s[0:1], s[10:11], 13
	v_lshrrev_b32_e32 v18, 6, v0
	v_and_b32_e32 v166, 15, v0
	v_and_b32_e32 v167, 48, v0
	v_readfirstlane_b32 s2, v18
	v_and_b32_e32 v168, 63, v0
	v_mul_u32_u24_e32 v169, 0x90, v166
	s_and_b32 s3, s2, 1
	s_lshr_b32 s4, s2, 1
	v_add_u32_e32 v169, v169, v167
	s_mul_i32 s5, s3, 0x1200
	s_lshl_b32 s12, s3, 12
	s_cmp_lt_u32 s4, 2
	s_cbranch_scc1 .Ls4_qh
	s_cmp_eq_u32 s4, 2
	s_cbranch_scc1 .Ls4_a
	s_add_u32 s14, s36, s0
	s_addc_u32 s15, s37, s1
	v_add_u32_e32 v170, s5, v169
	v_add_u32_e32 v171, 0x18c00, v169
	s_lshl_b32 s13, s3, 7
	v_add_u32_e32 v172, 0x27c00, v167
	v_add_u32_e32 v172, s13, v172
	v_lshl_add_u32 v173, v168, 3, s12
	ds_read_b128 v[2:5], v170 offset:36864
	ds_read_b128 v[6:9], v171 offset:0
	ds_read_b128 v[10:13], v170 offset:36928
	ds_read_b128 v[14:17], v171 offset:64
	ds_read_b128 v[174:177], v170 offset:46080
	ds_read_b128 v[178:181], v169 offset:55296
	ds_read_b128 v[240:243], v170 offset:46144
	ds_read_b128 v[244:247], v169 offset:55360
	ds_read_b128 v[218:221], v172 offset:0
	s_waitcnt lgkmcnt(7)
	v_mfma_f32_16x16x32_bf16 v[24:27], v[2:5], v[6:9], 0
	ds_read_b128 v[2:5], v170 offset:36864
	ds_read_b128 v[6:9], v171 offset:2304
	s_waitcnt lgkmcnt(7)
	v_mfma_f32_16x16x32_bf16 v[24:27], v[10:13], v[14:17], v[24:27]
	ds_read_b128 v[10:13], v170 offset:36928
	ds_read_b128 v[14:17], v171 offset:2368
	s_waitcnt lgkmcnt(7)
	v_mfma_f32_16x16x32_bf16 v[24:27], v[174:177], v[178:181], v[24:27]
	ds_read_b128 v[174:177], v170 offset:46080
	ds_read_b128 v[178:181], v169 offset:57600
	s_waitcnt lgkmcnt(7)
	v_mfma_f32_16x16x32_bf16 v[24:27], v[240:243], v[244:247], v[24:27]
	ds_read_b128 v[240:243], v170 offset:46144
	ds_read_b128 v[244:247], v169 offset:57664
	ds_read_b128 v[18:21], v172 offset:0
	s_waitcnt lgkmcnt(9)
	s_nop 3
	v_pk_mul_f32 v[24:25], v[24:25], v[218:219]
	v_pk_mul_f32 v[26:27], v[26:27], v[220:221]
	v_cvt_pk_bf16_f32 v32, v24, v25
	v_cvt_pk_bf16_f32 v33, v26, v27
	global_store_dwordx2 v173, v[32:33], s[14:15] offset:0
	s_waitcnt lgkmcnt(7)
	v_mfma_f32_16x16x32_bf16 v[28:31], v[2:5], v[6:9], 0
	ds_read_b128 v[2:5], v170 offset:36864
	ds_read_b128 v[6:9], v171 offset:4608
	s_waitcnt lgkmcnt(7)
	v_mfma_f32_16x16x32_bf16 v[28:31], v[10:13], v[14:17], v[28:31]
	ds_read_b128 v[10:13], v170 offset:36928
	ds_read_b128 v[14:17], v171 offset:4672
	s_waitcnt lgkmcnt(7)
	v_mfma_f32_16x16x32_bf16 v[28:31], v[174:177], v[178:181], v[28:31]
	ds_read_b128 v[174:177], v170 offset:46080
	ds_read_b128 v[178:181], v169 offset:59904
	s_waitcnt lgkmcnt(7)
	v_mfma_f32_16x16x32_bf16 v[28:31], v[240:243], v[244:247], v[28:31]
	ds_read_b128 v[240:243], v170 offset:46144
	ds_read_b128 v[244:247], v169 offset:59968
	ds_read_b128 v[218:221], v172 offset:0
	s_waitcnt lgkmcnt(9)
	s_nop 3
	v_pk_mul_f32 v[28:29], v[28:29], v[18:19]
	v_pk_mul_f32 v[30:31], v[30:31], v[20:21]
	v_cvt_pk_bf16_f32 v22, v28, v29
	v_cvt_pk_bf16_f32 v23, v30, v31
	global_store_dwordx2 v173, v[22:23], s[14:15] offset:512
	s_waitcnt lgkmcnt(7)
	v_mfma_f32_16x16x32_bf16 v[24:27], v[2:5], v[6:9], 0
	ds_read_b128 v[2:5], v170 offset:36864
	ds_read_b128 v[6:9], v171 offset:6912
	s_waitcnt lgkmcnt(7)
	v_mfma_f32_16x16x32_bf16 v[24:27], v[10:13], v[14:17], v[24:27]
	ds_read_b128 v[10:13], v170 offset:36928
	ds_read_b128 v[14:17], v171 offset:6976
	s_waitcnt lgkmcnt(7)
	v_mfma_f32_16x16x32_bf16 v[24:27], v[174:177], v[178:181], v[24:27]
	ds_read_b128 v[174:177], v170 offset:46080
	ds_read_b128 v[178:181], v169 offset:62208
	s_waitcnt lgkmcnt(7)
	v_mfma_f32_16x16x32_bf16 v[24:27], v[240:243], v[244:247], v[24:27]
	ds_read_b128 v[240:243], v170 offset:46144
	ds_read_b128 v[244:247], v169 offset:62272
	ds_read_b128 v[18:21], v172 offset:0
	s_waitcnt lgkmcnt(9)
	s_nop 3
	v_pk_mul_f32 v[24:25], v[24:25], v[218:219]
	v_pk_mul_f32 v[26:27], v[26:27], v[220:221]
	v_cvt_pk_bf16_f32 v32, v24, v25
	v_cvt_pk_bf16_f32 v33, v26, v27
	global_store_dwordx2 v173, v[32:33], s[14:15] offset:1024
	s_waitcnt lgkmcnt(7)
	v_mfma_f32_16x16x32_bf16 v[28:31], v[2:5], v[6:9], 0
	ds_read_b128 v[2:5], v170 offset:39168
	ds_read_b128 v[6:9], v171 offset:0
	s_waitcnt lgkmcnt(7)
	v_mfma_f32_16x16x32_bf16 v[28:31], v[10:13], v[14:17], v[28:31]
	ds_read_b128 v[10:13], v170 offset:39232
	ds_read_b128 v[14:17], v171 offset:64
	s_waitcnt lgkmcnt(7)
	v_mfma_f32_16x16x32_bf16 v[28:31], v[174:177], v[178:181], v[28:31]
	ds_read_b128 v[174:177], v170 offset:48384
	ds_read_b128 v[178:181], v169 offset:55296
	s_waitcnt lgkmcnt(7)
	v_mfma_f32_16x16x32_bf16 v[28:31], v[240:243], v[244:247], v[28:31]
	ds_read_b128 v[240:243], v170 offset:48448
	ds_read_b128 v[244:247], v169 offset:55360
	ds_read_b128 v[218:221], v172 offset:64
	s_waitcnt lgkmcnt(9)
	s_nop 3
	v_pk_mul_f32 v[28:29], v[28:29], v[18:19]
	v_pk_mul_f32 v[30:31], v[30:31], v[20:21]
	v_cvt_pk_bf16_f32 v22, v28, v29
	v_cvt_pk_bf16_f32 v23, v30, v31
	global_store_dwordx2 v173, v[22:23], s[14:15] offset:1536
	s_waitcnt lgkmcnt(7)
	v_mfma_f32_16x16x32_bf16 v[24:27], v[2:5], v[6:9], 0
	ds_read_b128 v[2:5], v170 offset:39168
	ds_read_b128 v[6:9], v171 offset:2304
	s_waitcnt lgkmcnt(7)
	v_mfma_f32_16x16x32_bf16 v[24:27], v[10:13], v[14:17], v[24:27]
	ds_read_b128 v[10:13], v170 offset:39232
	ds_read_b128 v[14:17], v171 offset:2368
	s_waitcnt lgkmcnt(7)
	v_mfma_f32_16x16x32_bf16 v[24:27], v[174:177], v[178:181], v[24:27]
	ds_read_b128 v[174:177], v170 offset:48384
	ds_read_b128 v[178:181], v169 offset:57600
	s_waitcnt lgkmcnt(7)
	v_mfma_f32_16x16x32_bf16 v[24:27], v[240:243], v[244:247], v[24:27]
	ds_read_b128 v[240:243], v170 offset:48448
	ds_read_b128 v[244:247], v169 offset:57664
	ds_read_b128 v[18:21], v172 offset:64
	s_waitcnt lgkmcnt(9)
	s_nop 3
	v_pk_mul_f32 v[24:25], v[24:25], v[218:219]
	v_pk_mul_f32 v[26:27], v[26:27], v[220:221]
	v_cvt_pk_bf16_f32 v32, v24, v25
	v_cvt_pk_bf16_f32 v33, v26, v27
	global_store_dwordx2 v173, v[32:33], s[14:15] offset:2048
	s_waitcnt lgkmcnt(7)
	v_mfma_f32_16x16x32_bf16 v[28:31], v[2:5], v[6:9], 0
	ds_read_b128 v[2:5], v170 offset:39168
	ds_read_b128 v[6:9], v171 offset:4608
	s_waitcnt lgkmcnt(7)
	v_mfma_f32_16x16x32_bf16 v[28:31], v[10:13], v[14:17], v[28:31]
	ds_read_b128 v[10:13], v170 offset:39232
	ds_read_b128 v[14:17], v171 offset:4672
	s_waitcnt lgkmcnt(7)
	v_mfma_f32_16x16x32_bf16 v[28:31], v[174:177], v[178:181], v[28:31]
	ds_read_b128 v[174:177], v170 offset:48384
	ds_read_b128 v[178:181], v169 offset:59904
	s_waitcnt lgkmcnt(7)
	v_mfma_f32_16x16x32_bf16 v[28:31], v[240:243], v[244:247], v[28:31]
	ds_read_b128 v[240:243], v170 offset:48448
	ds_read_b128 v[244:247], v169 offset:59968
	ds_read_b128 v[218:221], v172 offset:64
	s_waitcnt lgkmcnt(9)
	s_nop 3
	v_pk_mul_f32 v[28:29], v[28:29], v[18:19]
	v_pk_mul_f32 v[30:31], v[30:31], v[20:21]
	v_cvt_pk_bf16_f32 v22, v28, v29
	v_cvt_pk_bf16_f32 v23, v30, v31
	global_store_dwordx2 v173, v[22:23], s[14:15] offset:2560
	s_waitcnt lgkmcnt(7)
	v_mfma_f32_16x16x32_bf16 v[24:27], v[2:5], v[6:9], 0
	ds_read_b128 v[2:5], v170 offset:39168
	ds_read_b128 v[6:9], v171 offset:6912
	s_waitcnt lgkmcnt(7)
	v_mfma_f32_16x16x32_bf16 v[24:27], v[10:13], v[14:17], v[24:27]
	ds_read_b128 v[10:13], v170 offset:39232
	ds_read_b128 v[14:17], v171 offset:6976
	s_waitcnt lgkmcnt(7)
	v_mfma_f32_16x16x32_bf16 v[24:27], v[174:177], v[178:181], v[24:27]
	ds_read_b128 v[174:177], v170 offset:48384
	ds_read_b128 v[178:181], v169 offset:62208
	s_waitcnt lgkmcnt(7)
	v_mfma_f32_16x16x32_bf16 v[24:27], v[240:243], v[244:247], v[24:27]
	ds_read_b128 v[240:243], v170 offset:48448
	ds_read_b128 v[244:247], v169 offset:62272
	ds_read_b128 v[18:21], v172 offset:64
	s_waitcnt lgkmcnt(9)
	s_nop 3
	v_pk_mul_f32 v[24:25], v[24:25], v[218:219]
	v_pk_mul_f32 v[26:27], v[26:27], v[220:221]
	v_cvt_pk_bf16_f32 v32, v24, v25
	v_cvt_pk_bf16_f32 v33, v26, v27
	global_store_dwordx2 v173, v[32:33], s[14:15] offset:3072
	s_waitcnt lgkmcnt(7)
	v_mfma_f32_16x16x32_bf16 v[28:31], v[2:5], v[6:9], 0
	s_waitcnt lgkmcnt(5)
	v_mfma_f32_16x16x32_bf16 v[28:31], v[10:13], v[14:17], v[28:31]
	s_waitcnt lgkmcnt(3)
	v_mfma_f32_16x16x32_bf16 v[28:31], v[174:177], v[178:181], v[28:31]
	s_waitcnt lgkmcnt(1)
	v_mfma_f32_16x16x32_bf16 v[28:31], v[240:243], v[244:247], v[28:31]
	s_waitcnt lgkmcnt(0)
	s_nop 6
	v_pk_mul_f32 v[28:29], v[28:29], v[18:19]
	v_pk_mul_f32 v[30:31], v[30:31], v[20:21]
	v_cvt_pk_bf16_f32 v22, v28, v29
	v_cvt_pk_bf16_f32 v23, v30, v31
	global_store_dwordx2 v173, v[22:23], s[14:15] offset:3584
	s_branch .LBB0_600
.Ls4_a:
	s_add_u32 s14, s29, s0
	s_addc_u32 s15, s30, s1
	v_add_u32_e32 v170, s5, v169
	v_add_u32_e32 v170, 0x16800, v170
	v_lshlrev_b32_e32 v172, 2, v166
	v_add_u32_e32 v172, 0x27c00, v172
	v_lshl_add_u32 v173, v168, 4, s12
	v_lshrrev_b32_e32 v171, 2, v167
	v_sub_u32_e32 v171, v166, v171
	s_lshl_b32 s13, s3, 5
	v_subrev_u32_e32 v171, s13, v171
	ds_read_b128 v[2:5], v170 offset:0
	ds_read_b128 v[6:9], v169 offset:36864
	ds_read_b128 v[10:13], v170 offset:64
	ds_read_b128 v[14:17], v169 offset:36928
	ds_read_b32 v218, v172 offset:0
	ds_read_b128 v[174:177], v170 offset:0
	ds_read_b128 v[178:181], v169 offset:39168
	ds_read_b128 v[240:243], v170 offset:64
	ds_read_b128 v[244:247], v169 offset:39232
	ds_read_b32 v18, v172 offset:64
	v_add_u32_e32 v183, 0, v171
	v_cmp_eq_u32_e64 s[16:17], 0, v183
	v_cmp_eq_u32_e64 s[18:19], 1, v183
	v_cmp_eq_u32_e64 s[20:21], 2, v183
	v_cmp_eq_u32_e64 s[22:23], 3, v183
	v_cndmask_b32_e64 v248, 0, 1.0, s[16:17]
	v_cndmask_b32_e64 v249, 0, 1.0, s[18:19]
	v_cndmask_b32_e64 v184, 0, 1.0, s[20:21]
	v_cndmask_b32_e64 v185, 0, 1.0, s[22:23]
	s_waitcnt lgkmcnt(8)
	v_mfma_f32_16x16x32_bf16 v[24:27], v[2:5], v[6:9], 0
	ds_read_b128 v[2:5], v170 offset:0
	ds_read_b128 v[6:9], v169 offset:41472
	s_waitcnt lgkmcnt(8)
	v_mfma_f32_16x16x32_bf16 v[24:27], v[10:13], v[14:17], v[24:27]
	ds_read_b128 v[10:13], v170 offset:64
	ds_read_b128 v[14:17], v169 offset:41536
	s_waitcnt lgkmcnt(9)
	s_nop 4
	v_pk_add_f32 v[24:25], v[248:249], v[24:25]
	v_pk_add_f32 v[26:27], v[184:185], v[26:27]
	v_mul_f32_e32 v24, v218, v24
	v_mul_f32_e32 v25, v218, v25
	v_mul_f32_e32 v26, v218, v26
	v_mul_f32_e32 v27, v218, v27
	v_cvt_pk_bf16_f32 v32, v24, v25
	v_cvt_pk_bf16_f32 v33, v26, v27
	ds_read_b32 v218, v172 offset:128
	global_store_dwordx2 v173, v[32:33], s[14:15] offset:0
	v_add_u32_e32 v183, 16, v171
	v_cmp_eq_u32_e64 s[16:17], 0, v183
	v_cmp_eq_u32_e64 s[18:19], 1, v183
	v_cmp_eq_u32_e64 s[20:21], 2, v183
	v_cmp_eq_u32_e64 s[22:23], 3, v183
	v_cndmask_b32_e64 v248, 0, 1.0, s[16:17]
	v_cndmask_b32_e64 v249, 0, 1.0, s[18:19]
	v_cndmask_b32_e64 v184, 0, 1.0, s[20:21]
	v_cndmask_b32_e64 v185, 0, 1.0, s[22:23]
	s_waitcnt lgkmcnt(8)
	v_mfma_f32_16x16x32_bf16 v[28:31], v[174:177], v[178:181], 0
	ds_read_b128 v[174:177], v170 offset:0
	ds_read_b128 v[178:181], v169 offset:43776
	s_waitcnt lgkmcnt(8)
	v_mfma_f32_16x16x32_bf16 v[28:31], v[240:243], v[244:247], v[28:31]
	ds_read_b128 v[240:243], v170 offset:64
	ds_read_b128 v[244:247], v169 offset:43840
	s_waitcnt lgkmcnt(9)
	s_nop 4
	v_pk_add_f32 v[28:29], v[248:249], v[28:29]
	v_pk_add_f32 v[30:31], v[184:185], v[30:31]
	v_mul_f32_e32 v28, v18, v28
	v_mul_f32_e32 v29, v18, v29
	v_mul_f32_e32 v30, v18, v30
	v_mul_f32_e32 v31, v18, v31
	v_cvt_pk_bf16_f32 v22, v28, v29
	v_cvt_pk_bf16_f32 v23, v30, v31
	ds_read_b32 v18, v172 offset:192
	global_store_dwordx2 v173, v[22:23], s[14:15] offset:1024
	v_add_u32_e32 v183, 32, v171
	v_cmp_eq_u32_e64 s[16:17], 0, v183
	v_cmp_eq_u32_e64 s[18:19], 1, v183
	v_cmp_eq_u32_e64 s[20:21], 2, v183
	v_cmp_eq_u32_e64 s[22:23], 3, v183
	v_cndmask_b32_e64 v248, 0, 1.0, s[16:17]
	v_cndmask_b32_e64 v249, 0, 1.0, s[18:19]
	v_cndmask_b32_e64 v184, 0, 1.0, s[20:21]
	v_cndmask_b32_e64 v185, 0, 1.0, s[22:23]
	s_waitcnt lgkmcnt(8)
	v_mfma_f32_16x16x32_bf16 v[24:27], v[2:5], v[6:9], 0
	ds_read_b128 v[2:5], v170 offset:2304
	ds_read_b128 v[6:9], v169 offset:36864
	s_waitcnt lgkmcnt(8)
	v_mfma_f32_16x16x32_bf16 v[24:27], v[10:13], v[14:17], v[24:27]
	ds_read_b128 v[10:13], v170 offset:2368
	ds_read_b128 v[14:17], v169 offset:36928
	s_waitcnt lgkmcnt(9)
	s_nop 4
	v_pk_add_f32 v[24:25], v[248:249], v[24:25]
	v_pk_add_f32 v[26:27], v[184:185], v[26:27]
	v_mul_f32_e32 v24, v218, v24
	v_mul_f32_e32 v25, v218, v25
	v_mul_f32_e32 v26, v218, v26
	v_mul_f32_e32 v27, v218, v27
	v_cvt_pk_bf16_f32 v32, v24, v25
	v_cvt_pk_bf16_f32 v33, v26, v27
	ds_read_b32 v218, v172 offset:0
	global_store_dwordx2 v173, v[32:33], s[14:15] offset:2048
	v_add_u32_e32 v183, 48, v171
	v_cmp_eq_u32_e64 s[16:17], 0, v183
	v_cmp_eq_u32_e64 s[18:19], 1, v183
	v_cmp_eq_u32_e64 s[20:21], 2, v183
	v_cmp_eq_u32_e64 s[22:23], 3, v183
	v_cndmask_b32_e64 v248, 0, 1.0, s[16:17]
	v_cndmask_b32_e64 v249, 0, 1.0, s[18:19]
	v_cndmask_b32_e64 v184, 0, 1.0, s[20:21]
	v_cndmask_b32_e64 v185, 0, 1.0, s[22:23]
	s_waitcnt lgkmcnt(8)
	v_mfma_f32_16x16x32_bf16 v[28:31], v[174:177], v[178:181], 0
	ds_read_b128 v[174:177], v170 offset:2304
	ds_read_b128 v[178:181], v169 offset:39168
	s_waitcnt lgkmcnt(8)
	v_mfma_f32_16x16x32_bf16 v[28:31], v[240:243], v[244:247], v[28:31]
	ds_read_b128 v[240:243], v170 offset:2368
	ds_read_b128 v[244:247], v169 offset:39232
	s_waitcnt lgkmcnt(9)
	s_nop 4
	v_pk_add_f32 v[28:29], v[248:249], v[28:29]
	v_pk_add_f32 v[30:31], v[184:185], v[30:31]
	v_mul_f32_e32 v28, v18, v28
	v_mul_f32_e32 v29, v18, v29
	v_mul_f32_e32 v30, v18, v30
	v_mul_f32_e32 v31, v18, v31
	v_cvt_pk_bf16_f32 v22, v28, v29
	v_cvt_pk_bf16_f32 v23, v30, v31
	ds_read_b32 v18, v172 offset:64
	global_store_dwordx2 v173, v[22:23], s[14:15] offset:3072
	v_add_u32_e32 v183, -16, v171
	v_cmp_eq_u32_e64 s[16:17], 0, v183
	v_cmp_eq_u32_e64 s[18:19], 1, v183
	v_cmp_eq_u32_e64 s[20:21], 2, v183
	v_cmp_eq_u32_e64 s[22:23], 3, v183
	v_cndmask_b32_e64 v248, 0, 1.0, s[16:17]
	v_cndmask_b32_e64 v249, 0, 1.0, s[18:19]
	v_cndmask_b32_e64 v184, 0, 1.0, s[20:21]
	v_cndmask_b32_e64 v185, 0, 1.0, s[22:23]
	s_waitcnt lgkmcnt(8)
	v_mfma_f32_16x16x32_bf16 v[24:27], v[2:5], v[6:9], 0
	ds_read_b128 v[2:5], v170 offset:2304
	ds_read_b128 v[6:9], v169 offset:41472
	s_waitcnt lgkmcnt(8)
	v_mfma_f32_16x16x32_bf16 v[24:27], v[10:13], v[14:17], v[24:27]
	ds_read_b128 v[10:13], v170 offset:2368
	ds_read_b128 v[14:17], v169 offset:41536
	s_waitcnt lgkmcnt(9)
	s_nop 4
	v_pk_add_f32 v[24:25], v[248:249], v[24:25]
	v_pk_add_f32 v[26:27], v[184:185], v[26:27]
	v_mul_f32_e32 v24, v218, v24
	v_mul_f32_e32 v25, v218, v25
	v_mul_f32_e32 v26, v218, v26
	v_mul_f32_e32 v27, v218, v27
	v_cvt_pk_bf16_f32 v32, v24, v25
	v_cvt_pk_bf16_f32 v33, v26, v27
	ds_read_b32 v218, v172 offset:128
	global_store_dwordx2 v173, v[32:33], s[14:15] offset:8
	v_add_u32_e32 v183, 0, v171
	v_cmp_eq_u32_e64 s[16:17], 0, v183
	v_cmp_eq_u32_e64 s[18:19], 1, v183
	v_cmp_eq_u32_e64 s[20:21], 2, v183
	v_cmp_eq_u32_e64 s[22:23], 3, v183
	v_cndmask_b32_e64 v248, 0, 1.0, s[16:17]
	v_cndmask_b32_e64 v249, 0, 1.0, s[18:19]
	v_cndmask_b32_e64 v184, 0, 1.0, s[20:21]
	v_cndmask_b32_e64 v185, 0, 1.0, s[22:23]
	s_waitcnt lgkmcnt(8)
	v_mfma_f32_16x16x32_bf16 v[28:31], v[174:177], v[178:181], 0
	ds_read_b128 v[174:177], v170 offset:2304
	ds_read_b128 v[178:181], v169 offset:43776
	s_waitcnt lgkmcnt(8)
	v_mfma_f32_16x16x32_bf16 v[28:31], v[240:243], v[244:247], v[28:31]
	ds_read_b128 v[240:243], v170 offset:2368
	ds_read_b128 v[244:247], v169 offset:43840
	s_waitcnt lgkmcnt(9)
	s_nop 4
	v_pk_add_f32 v[28:29], v[248:249], v[28:29]
	v_pk_add_f32 v[30:31], v[184:185], v[30:31]
	v_mul_f32_e32 v28, v18, v28
	v_mul_f32_e32 v29, v18, v29
	v_mul_f32_e32 v30, v18, v30
	v_mul_f32_e32 v31, v18, v31
	v_cvt_pk_bf16_f32 v22, v28, v29
	v_cvt_pk_bf16_f32 v23, v30, v31
	ds_read_b32 v18, v172 offset:192
	global_store_dwordx2 v173, v[22:23], s[14:15] offset:1032
	v_add_u32_e32 v183, 16, v171
	v_cmp_eq_u32_e64 s[16:17], 0, v183
	v_cmp_eq_u32_e64 s[18:19], 1, v183
	v_cmp_eq_u32_e64 s[20:21], 2, v183
	v_cmp_eq_u32_e64 s[22:23], 3, v183
	v_cndmask_b32_e64 v248, 0, 1.0, s[16:17]
	v_cndmask_b32_e64 v249, 0, 1.0, s[18:19]
	v_cndmask_b32_e64 v184, 0, 1.0, s[20:21]
	v_cndmask_b32_e64 v185, 0, 1.0, s[22:23]
	s_waitcnt lgkmcnt(8)
	v_mfma_f32_16x16x32_bf16 v[24:27], v[2:5], v[6:9], 0
	s_waitcnt lgkmcnt(6)
	v_mfma_f32_16x16x32_bf16 v[24:27], v[10:13], v[14:17], v[24:27]
	s_waitcnt lgkmcnt(5)
	s_nop 6
	v_pk_add_f32 v[24:25], v[248:249], v[24:25]
	v_pk_add_f32 v[26:27], v[184:185], v[26:27]
	v_mul_f32_e32 v24, v218, v24
	v_mul_f32_e32 v25, v218, v25
	v_mul_f32_e32 v26, v218, v26
	v_mul_f32_e32 v27, v218, v27
	v_cvt_pk_bf16_f32 v32, v24, v25
	v_cvt_pk_bf16_f32 v33, v26, v27
	global_store_dwordx2 v173, v[32:33], s[14:15] offset:2056
	v_add_u32_e32 v183, 32, v171
	v_cmp_eq_u32_e64 s[16:17], 0, v183
	v_cmp_eq_u32_e64 s[18:19], 1, v183
	v_cmp_eq_u32_e64 s[20:21], 2, v183
	v_cmp_eq_u32_e64 s[22:23], 3, v183
	v_cndmask_b32_e64 v248, 0, 1.0, s[16:17]
	v_cndmask_b32_e64 v249, 0, 1.0, s[18:19]
	v_cndmask_b32_e64 v184, 0, 1.0, s[20:21]
	v_cndmask_b32_e64 v185, 0, 1.0, s[22:23]
	s_waitcnt lgkmcnt(3)
	v_mfma_f32_16x16x32_bf16 v[28:31], v[174:177], v[178:181], 0
	s_waitcnt lgkmcnt(1)
	v_mfma_f32_16x16x32_bf16 v[28:31], v[240:243], v[244:247], v[28:31]
	s_waitcnt lgkmcnt(0)
	s_nop 6
	v_pk_add_f32 v[28:29], v[248:249], v[28:29]
	v_pk_add_f32 v[30:31], v[184:185], v[30:31]
	v_mul_f32_e32 v28, v18, v28
	v_mul_f32_e32 v29, v18, v29
	v_mul_f32_e32 v30, v18, v30
	v_mul_f32_e32 v31, v18, v31
	v_cvt_pk_bf16_f32 v22, v28, v29
	v_cvt_pk_bf16_f32 v23, v30, v31
	global_store_dwordx2 v173, v[22:23], s[14:15] offset:3080
	s_branch .LBB0_600
.Ls4_qh:
	s_cmp_eq_u32 s4, 0
	s_cbranch_scc1 .Ls4_q
	s_add_u32 s14, s31, s0
	s_addc_u32 s15, s35, s1
	v_add_u32_e32 v170, s5, v169
	v_add_u32_e32 v170, 0x12000, v170
	v_add_u32_e32 v171, 0x18c00, v169
	v_lshl_add_u32 v173, v168, 3, s12
	ds_read_b128 v[2:5], v170 offset:0
	ds_read_b128 v[6:9], v171 offset:0
	ds_read_b128 v[10:13], v170 offset:64
	ds_read_b128 v[14:17], v171 offset:64
	ds_read_b128 v[174:177], v170 offset:9216
	ds_read_b128 v[178:181], v169 offset:55296
	ds_read_b128 v[240:243], v170 offset:9280
	ds_read_b128 v[244:247], v169 offset:55360
	s_waitcnt lgkmcnt(6)
	v_mfma_f32_16x16x32_bf16 v[24:27], v[2:5], v[6:9], 0
	ds_read_b128 v[2:5], v170 offset:0
	ds_read_b128 v[6:9], v171 offset:2304
	s_waitcnt lgkmcnt(6)
	v_mfma_f32_16x16x32_bf16 v[24:27], v[10:13], v[14:17], v[24:27]
	ds_read_b128 v[10:13], v170 offset:64
	ds_read_b128 v[14:17], v171 offset:2368
	s_waitcnt lgkmcnt(6)
	v_mfma_f32_16x16x32_bf16 v[24:27], v[174:177], v[178:181], v[24:27]
	ds_read_b128 v[174:177], v170 offset:9216
	ds_read_b128 v[178:181], v169 offset:57600
	s_waitcnt lgkmcnt(6)
	v_mfma_f32_16x16x32_bf16 v[24:27], v[240:243], v[244:247], v[24:27]
	ds_read_b128 v[240:243], v170 offset:9280
	ds_read_b128 v[244:247], v169 offset:57664
	s_nop 5
	v_cvt_pk_bf16_f32 v32, v24, v25
	v_cvt_pk_bf16_f32 v33, v26, v27
	global_store_dwordx2 v173, v[32:33], s[14:15] offset:0
	s_waitcnt lgkmcnt(6)
	v_mfma_f32_16x16x32_bf16 v[28:31], v[2:5], v[6:9], 0
	ds_read_b128 v[2:5], v170 offset:0
	ds_read_b128 v[6:9], v171 offset:4608
	s_waitcnt lgkmcnt(6)
	v_mfma_f32_16x16x32_bf16 v[28:31], v[10:13], v[14:17], v[28:31]
	ds_read_b128 v[10:13], v170 offset:64
	ds_read_b128 v[14:17], v171 offset:4672
	s_waitcnt lgkmcnt(6)
	v_mfma_f32_16x16x32_bf16 v[28:31], v[174:177], v[178:181], v[28:31]
	ds_read_b128 v[174:177], v170 offset:9216
	ds_read_b128 v[178:181], v169 offset:59904
	s_waitcnt lgkmcnt(6)
	v_mfma_f32_16x16x32_bf16 v[28:31], v[240:243], v[244:247], v[28:31]
	ds_read_b128 v[240:243], v170 offset:9280
	ds_read_b128 v[244:247], v169 offset:59968
	s_nop 5
	v_cvt_pk_bf16_f32 v22, v28, v29
	v_cvt_pk_bf16_f32 v23, v30, v31
	global_store_dwordx2 v173, v[22:23], s[14:15] offset:512
	s_waitcnt lgkmcnt(6)
	v_mfma_f32_16x16x32_bf16 v[24:27], v[2:5], v[6:9], 0
	ds_read_b128 v[2:5], v170 offset:0
	ds_read_b128 v[6:9], v171 offset:6912
	s_waitcnt lgkmcnt(6)
	v_mfma_f32_16x16x32_bf16 v[24:27], v[10:13], v[14:17], v[24:27]
	ds_read_b128 v[10:13], v170 offset:64
	ds_read_b128 v[14:17], v171 offset:6976
	s_waitcnt lgkmcnt(6)
	v_mfma_f32_16x16x32_bf16 v[24:27], v[174:177], v[178:181], v[24:27]
	ds_read_b128 v[174:177], v170 offset:9216
	ds_read_b128 v[178:181], v169 offset:62208
	s_waitcnt lgkmcnt(6)
	v_mfma_f32_16x16x32_bf16 v[24:27], v[240:243], v[244:247], v[24:27]
	ds_read_b128 v[240:243], v170 offset:9280
	ds_read_b128 v[244:247], v169 offset:62272
	s_nop 5
	v_cvt_pk_bf16_f32 v32, v24, v25
	v_cvt_pk_bf16_f32 v33, v26, v27
	global_store_dwordx2 v173, v[32:33], s[14:15] offset:1024
	s_waitcnt lgkmcnt(6)
	v_mfma_f32_16x16x32_bf16 v[28:31], v[2:5], v[6:9], 0
	ds_read_b128 v[2:5], v170 offset:2304
	ds_read_b128 v[6:9], v171 offset:0
	s_waitcnt lgkmcnt(6)
	v_mfma_f32_16x16x32_bf16 v[28:31], v[10:13], v[14:17], v[28:31]
	ds_read_b128 v[10:13], v170 offset:2368
	ds_read_b128 v[14:17], v171 offset:64
	s_waitcnt lgkmcnt(6)
	v_mfma_f32_16x16x32_bf16 v[28:31], v[174:177], v[178:181], v[28:31]
	ds_read_b128 v[174:177], v170 offset:11520
	ds_read_b128 v[178:181], v169 offset:55296
	s_waitcnt lgkmcnt(6)
	v_mfma_f32_16x16x32_bf16 v[28:31], v[240:243], v[244:247], v[28:31]
	ds_read_b128 v[240:243], v170 offset:11584
	ds_read_b128 v[244:247], v169 offset:55360
	s_nop 5
	v_cvt_pk_bf16_f32 v22, v28, v29
	v_cvt_pk_bf16_f32 v23, v30, v31
	global_store_dwordx2 v173, v[22:23], s[14:15] offset:1536
	s_waitcnt lgkmcnt(6)
	v_mfma_f32_16x16x32_bf16 v[24:27], v[2:5], v[6:9], 0
	ds_read_b128 v[2:5], v170 offset:2304
	ds_read_b128 v[6:9], v171 offset:2304
	s_waitcnt lgkmcnt(6)
	v_mfma_f32_16x16x32_bf16 v[24:27], v[10:13], v[14:17], v[24:27]
	ds_read_b128 v[10:13], v170 offset:2368
	ds_read_b128 v[14:17], v171 offset:2368
	s_waitcnt lgkmcnt(6)
	v_mfma_f32_16x16x32_bf16 v[24:27], v[174:177], v[178:181], v[24:27]
	ds_read_b128 v[174:177], v170 offset:11520
	ds_read_b128 v[178:181], v169 offset:57600
	s_waitcnt lgkmcnt(6)
	v_mfma_f32_16x16x32_bf16 v[24:27], v[240:243], v[244:247], v[24:27]
	ds_read_b128 v[240:243], v170 offset:11584
	ds_read_b128 v[244:247], v169 offset:57664
	s_nop 5
	v_cvt_pk_bf16_f32 v32, v24, v25
	v_cvt_pk_bf16_f32 v33, v26, v27
	global_store_dwordx2 v173, v[32:33], s[14:15] offset:2048
	s_waitcnt lgkmcnt(6)
	v_mfma_f32_16x16x32_bf16 v[28:31], v[2:5], v[6:9], 0
	ds_read_b128 v[2:5], v170 offset:2304
	ds_read_b128 v[6:9], v171 offset:4608
	s_waitcnt lgkmcnt(6)
	v_mfma_f32_16x16x32_bf16 v[28:31], v[10:13], v[14:17], v[28:31]
	ds_read_b128 v[10:13], v170 offset:2368
	ds_read_b128 v[14:17], v171 offset:4672
	s_waitcnt lgkmcnt(6)
	v_mfma_f32_16x16x32_bf16 v[28:31], v[174:177], v[178:181], v[28:31]
	ds_read_b128 v[174:177], v170 offset:11520
	ds_read_b128 v[178:181], v169 offset:59904
	s_waitcnt lgkmcnt(6)
	v_mfma_f32_16x16x32_bf16 v[28:31], v[240:243], v[244:247], v[28:31]
	ds_read_b128 v[240:243], v170 offset:11584
	ds_read_b128 v[244:247], v169 offset:59968
	s_nop 5
	v_cvt_pk_bf16_f32 v22, v28, v29
	v_cvt_pk_bf16_f32 v23, v30, v31
	global_store_dwordx2 v173, v[22:23], s[14:15] offset:2560
	s_waitcnt lgkmcnt(6)
	v_mfma_f32_16x16x32_bf16 v[24:27], v[2:5], v[6:9], 0
	ds_read_b128 v[2:5], v170 offset:2304
	ds_read_b128 v[6:9], v171 offset:6912
	s_waitcnt lgkmcnt(6)
	v_mfma_f32_16x16x32_bf16 v[24:27], v[10:13], v[14:17], v[24:27]
	ds_read_b128 v[10:13], v170 offset:2368
	ds_read_b128 v[14:17], v171 offset:6976
	s_waitcnt lgkmcnt(6)
	v_mfma_f32_16x16x32_bf16 v[24:27], v[174:177], v[178:181], v[24:27]
	ds_read_b128 v[174:177], v170 offset:11520
	ds_read_b128 v[178:181], v169 offset:62208
	s_waitcnt lgkmcnt(6)
	v_mfma_f32_16x16x32_bf16 v[24:27], v[240:243], v[244:247], v[24:27]
	ds_read_b128 v[240:243], v170 offset:11584
	ds_read_b128 v[244:247], v169 offset:62272
	s_nop 5
	v_cvt_pk_bf16_f32 v32, v24, v25
	v_cvt_pk_bf16_f32 v33, v26, v27
	global_store_dwordx2 v173, v[32:33], s[14:15] offset:3072
	s_waitcnt lgkmcnt(6)
	v_mfma_f32_16x16x32_bf16 v[28:31], v[2:5], v[6:9], 0
	s_waitcnt lgkmcnt(4)
	v_mfma_f32_16x16x32_bf16 v[28:31], v[10:13], v[14:17], v[28:31]
	s_waitcnt lgkmcnt(2)
	v_mfma_f32_16x16x32_bf16 v[28:31], v[174:177], v[178:181], v[28:31]
	s_waitcnt lgkmcnt(0)
	v_mfma_f32_16x16x32_bf16 v[28:31], v[240:243], v[244:247], v[28:31]
	s_nop 7
	v_cvt_pk_bf16_f32 v22, v28, v29
	v_cvt_pk_bf16_f32 v23, v30, v31
	global_store_dwordx2 v173, v[22:23], s[14:15] offset:3584
	s_branch .LBB0_600
.Ls4_q:
	s_add_u32 s14, s27, s0
	s_addc_u32 s15, s28, s1
	v_add_u32_e32 v170, s5, v169
	v_add_u32_e32 v170, 0x16800, v170
	v_add_u32_e32 v171, 0x12000, v169
	v_mul_u32_u24_e32 v172, 0x90, v166
	v_lshrrev_b32_e32 v183, 1, v167
	s_lshl_b32 s13, s3, 6
	v_add3_u32 v172, v172, v183, s13
	v_lshl_add_u32 v173, v168, 4, s12
	ds_read_b128 v[2:5], v170 offset:0
	ds_read_b128 v[6:9], v171 offset:0
	ds_read_b128 v[10:13], v170 offset:64
	ds_read_b128 v[14:17], v171 offset:64
	ds_read_b64 v[218:219], v172 offset:27648
	ds_read_b128 v[174:177], v170 offset:0
	ds_read_b128 v[178:181], v171 offset:2304
	ds_read_b128 v[240:243], v170 offset:64
	ds_read_b128 v[244:247], v171 offset:2368
	ds_read_b64 v[18:19], v172 offset:29952
	s_waitcnt lgkmcnt(8)
	v_mfma_f32_16x16x32_bf16 v[24:27], v[2:5], v[6:9], 0
	ds_read_b128 v[2:5], v170 offset:0
	ds_read_b128 v[6:9], v171 offset:4608
	s_waitcnt lgkmcnt(8)
	v_mfma_f32_16x16x32_bf16 v[24:27], v[10:13], v[14:17], v[24:27]
	ds_read_b128 v[10:13], v170 offset:64
	ds_read_b128 v[14:17], v171 offset:4672
	s_waitcnt lgkmcnt(9)
	s_nop 4
	v_lshlrev_b32_e32 v248, 16, v218
	v_and_b32_e32 v249, 0xffff0000, v218
	v_lshlrev_b32_e32 v184, 16, v219
	v_and_b32_e32 v185, 0xffff0000, v219
	v_pk_add_f32 v[24:25], v[24:25], v[248:249]
	v_pk_add_f32 v[26:27], v[26:27], v[184:185]
	v_cvt_pk_bf16_f32 v32, v24, v25
	v_cvt_pk_bf16_f32 v33, v26, v27
	ds_read_b64 v[218:219], v172 offset:32256
	global_store_dwordx2 v173, v[32:33], s[14:15] offset:0
	s_waitcnt lgkmcnt(8)
	v_mfma_f32_16x16x32_bf16 v[28:31], v[174:177], v[178:181], 0
	ds_read_b128 v[174:177], v170 offset:0
	ds_read_b128 v[178:181], v171 offset:6912
	s_waitcnt lgkmcnt(8)
	v_mfma_f32_16x16x32_bf16 v[28:31], v[240:243], v[244:247], v[28:31]
	ds_read_b128 v[240:243], v170 offset:64
	ds_read_b128 v[244:247], v171 offset:6976
	s_waitcnt lgkmcnt(9)
	s_nop 4
	v_lshlrev_b32_e32 v248, 16, v18
	v_and_b32_e32 v249, 0xffff0000, v18
	v_lshlrev_b32_e32 v184, 16, v19
	v_and_b32_e32 v185, 0xffff0000, v19
	v_pk_add_f32 v[28:29], v[28:29], v[248:249]
	v_pk_add_f32 v[30:31], v[30:31], v[184:185]
	v_cvt_pk_bf16_f32 v22, v28, v29
	v_cvt_pk_bf16_f32 v23, v30, v31
	ds_read_b64 v[18:19], v172 offset:34560
	global_store_dwordx2 v173, v[22:23], s[14:15] offset:1024
	s_waitcnt lgkmcnt(8)
	v_mfma_f32_16x16x32_bf16 v[24:27], v[2:5], v[6:9], 0
	ds_read_b128 v[2:5], v170 offset:2304
	ds_read_b128 v[6:9], v171 offset:0
	s_waitcnt lgkmcnt(8)
	v_mfma_f32_16x16x32_bf16 v[24:27], v[10:13], v[14:17], v[24:27]
	ds_read_b128 v[10:13], v170 offset:2368
	ds_read_b128 v[14:17], v171 offset:64
	s_waitcnt lgkmcnt(9)
	s_nop 4
	v_lshlrev_b32_e32 v248, 16, v218
	v_and_b32_e32 v249, 0xffff0000, v218
	v_lshlrev_b32_e32 v184, 16, v219
	v_and_b32_e32 v185, 0xffff0000, v219
	v_pk_add_f32 v[24:25], v[24:25], v[248:249]
	v_pk_add_f32 v[26:27], v[26:27], v[184:185]
	v_cvt_pk_bf16_f32 v32, v24, v25
	v_cvt_pk_bf16_f32 v33, v26, v27
	ds_read_b64 v[218:219], v172 offset:27680
	global_store_dwordx2 v173, v[32:33], s[14:15] offset:2048
	s_waitcnt lgkmcnt(8)
	v_mfma_f32_16x16x32_bf16 v[28:31], v[174:177], v[178:181], 0
	ds_read_b128 v[174:177], v170 offset:2304
	ds_read_b128 v[178:181], v171 offset:2304
	s_waitcnt lgkmcnt(8)
	v_mfma_f32_16x16x32_bf16 v[28:31], v[240:243], v[244:247], v[28:31]
	ds_read_b128 v[240:243], v170 offset:2368
	ds_read_b128 v[244:247], v171 offset:2368
	s_waitcnt lgkmcnt(9)
	s_nop 4
	v_lshlrev_b32_e32 v248, 16, v18
	v_and_b32_e32 v249, 0xffff0000, v18
	v_lshlrev_b32_e32 v184, 16, v19
	v_and_b32_e32 v185, 0xffff0000, v19
	v_pk_add_f32 v[28:29], v[28:29], v[248:249]
	v_pk_add_f32 v[30:31], v[30:31], v[184:185]
	v_cvt_pk_bf16_f32 v22, v28, v29
	v_cvt_pk_bf16_f32 v23, v30, v31
	ds_read_b64 v[18:19], v172 offset:29984
	global_store_dwordx2 v173, v[22:23], s[14:15] offset:3072
	s_waitcnt lgkmcnt(8)
	v_mfma_f32_16x16x32_bf16 v[24:27], v[2:5], v[6:9], 0
	ds_read_b128 v[2:5], v170 offset:2304
	ds_read_b128 v[6:9], v171 offset:4608
	s_waitcnt lgkmcnt(8)
	v_mfma_f32_16x16x32_bf16 v[24:27], v[10:13], v[14:17], v[24:27]
	ds_read_b128 v[10:13], v170 offset:2368
	ds_read_b128 v[14:17], v171 offset:4672
	s_waitcnt lgkmcnt(9)
	s_nop 4
	v_lshlrev_b32_e32 v248, 16, v218
	v_and_b32_e32 v249, 0xffff0000, v218
	v_lshlrev_b32_e32 v184, 16, v219
	v_and_b32_e32 v185, 0xffff0000, v219
	v_pk_add_f32 v[24:25], v[24:25], v[248:249]
	v_pk_add_f32 v[26:27], v[26:27], v[184:185]
	v_cvt_pk_bf16_f32 v32, v24, v25
	v_cvt_pk_bf16_f32 v33, v26, v27
	ds_read_b64 v[218:219], v172 offset:32288
	global_store_dwordx2 v173, v[32:33], s[14:15] offset:8
	s_waitcnt lgkmcnt(8)
	v_mfma_f32_16x16x32_bf16 v[28:31], v[174:177], v[178:181], 0
	ds_read_b128 v[174:177], v170 offset:2304
	ds_read_b128 v[178:181], v171 offset:6912
	s_waitcnt lgkmcnt(8)
	v_mfma_f32_16x16x32_bf16 v[28:31], v[240:243], v[244:247], v[28:31]
	ds_read_b128 v[240:243], v170 offset:2368
	ds_read_b128 v[244:247], v171 offset:6976
	s_waitcnt lgkmcnt(9)
	s_nop 4
	v_lshlrev_b32_e32 v248, 16, v18
	v_and_b32_e32 v249, 0xffff0000, v18
	v_lshlrev_b32_e32 v184, 16, v19
	v_and_b32_e32 v185, 0xffff0000, v19
	v_pk_add_f32 v[28:29], v[28:29], v[248:249]
	v_pk_add_f32 v[30:31], v[30:31], v[184:185]
	v_cvt_pk_bf16_f32 v22, v28, v29
	v_cvt_pk_bf16_f32 v23, v30, v31
	ds_read_b64 v[18:19], v172 offset:34592
	global_store_dwordx2 v173, v[22:23], s[14:15] offset:1032
	s_waitcnt lgkmcnt(8)
	v_mfma_f32_16x16x32_bf16 v[24:27], v[2:5], v[6:9], 0
	s_waitcnt lgkmcnt(6)
	v_mfma_f32_16x16x32_bf16 v[24:27], v[10:13], v[14:17], v[24:27]
	s_waitcnt lgkmcnt(5)
	s_nop 6
	v_lshlrev_b32_e32 v248, 16, v218
	v_and_b32_e32 v249, 0xffff0000, v218
	v_lshlrev_b32_e32 v184, 16, v219
	v_and_b32_e32 v185, 0xffff0000, v219
	v_pk_add_f32 v[24:25], v[24:25], v[248:249]
	v_pk_add_f32 v[26:27], v[26:27], v[184:185]
	v_cvt_pk_bf16_f32 v32, v24, v25
	v_cvt_pk_bf16_f32 v33, v26, v27
	global_store_dwordx2 v173, v[32:33], s[14:15] offset:2056
	s_waitcnt lgkmcnt(3)
	v_mfma_f32_16x16x32_bf16 v[28:31], v[174:177], v[178:181], 0
	s_waitcnt lgkmcnt(1)
	v_mfma_f32_16x16x32_bf16 v[28:31], v[240:243], v[244:247], v[28:31]
	s_waitcnt lgkmcnt(0)
	s_nop 6
	v_lshlrev_b32_e32 v248, 16, v18
	v_and_b32_e32 v249, 0xffff0000, v18
	v_lshlrev_b32_e32 v184, 16, v19
	v_and_b32_e32 v185, 0xffff0000, v19
	v_pk_add_f32 v[28:29], v[28:29], v[248:249]
	v_pk_add_f32 v[30:31], v[30:31], v[184:185]
	v_cvt_pk_bf16_f32 v22, v28, v29
	v_cvt_pk_bf16_f32 v23, v30, v31
	global_store_dwordx2 v173, v[22:23], s[14:15] offset:3080
	s_branch .LBB0_600
